# cache-policy: attention Q rows (read once) loaded non-temporally, on top of nt gathers
# speedup vs baseline: 1.0086x; 1.0035x over previous
.LBB0_1063:
	s_mul_hi_i32 s26, s13, 0x55555556
	s_lshr_b32 s27, s26, 31
	s_add_i32 s28, s26, s27
	s_mul_i32 s27, s58, 0x1100000
	s_mul_hi_i32 s26, s58, 0x1100000
	s_add_u32 s29, s66, s27
	s_addc_u32 s34, s67, s26
	s_and_b64 s[26:27], exec, s[24:25]
	s_movk_i32 s26, 0xb00
	s_cselect_b32 s26, 0x600, s26
	s_add_u32 s29, s29, s26
	s_addc_u32 s34, s34, 0
	s_lshl_b32 s26, s13, 6
	s_ashr_i32 s27, s26, 31
	s_lshl_b64 s[26:27], s[26:27], 1
	s_add_u32 s40, s29, s26
	s_addc_u32 s41, s34, s27
	s_lshl_b32 s12, s12, 4
	s_lshl_b32 s13, s58, 1
	s_add_i32 s12, s12, s28
	s_add_i32 s12, s12, s13
	s_mul_hi_i32 s13, s12, 0x88000
	s_mul_i32 s12, s12, 0x88000
	s_waitcnt lgkmcnt(0)
	s_add_u32 s8, s8, s12
	s_addc_u32 s9, s9, s13
	s_add_u32 s10, s10, s12
	s_waitcnt vmcnt(11)
	v_mbcnt_lo_u32_b32 v36, -1, 0
	v_mbcnt_hi_u32_b32 v36, -1, v36
	s_getreg_b32 s12, hwreg(HW_REG_HW_ID, 0, 6)
	s_addc_u32 s11, s11, s13
	s_lshl_b32 s12, s12, 2
	s_and_b32 s12, s12, 0xfc
	s_or_b32 s12, s12, 0x27100
	v_mov_b32_e32 v0, s12
	ds_read_b32 v0, v0
	s_and_b64 vcc, s[6:7], s[24:25]
	v_and_b32_e32 v211, 63, v36
	v_and_b32_e32 v231, 31, v36
	v_bfe_u32 v232, v36, 5, 1
	s_waitcnt lgkmcnt(0)
	v_readfirstlane_b32 s12, v0
	v_lshlrev_b32_e32 v0, 7, v211
	v_lshl_add_u64 v[2:3], s[8:9], 0, v[0:1]
	v_lshl_or_b32 v4, s12, 6, v36
	v_bfe_u32 v0, v36, 2, 4
	v_readfirstlane_b32 s13, v4
	s_ashr_i32 s89, s13, 6
	s_lshl_b32 s37, s89, 5
	s_add_i32 s28, s37, s36
	s_ashr_i32 s29, s28, 31
	s_lshl_b64 s[34:35], s[28:29], 12
	s_add_u32 s34, s40, s34
	s_addc_u32 s35, s41, s35
	s_lshl_b32 s8, s89, 3
	s_ashr_i32 s9, s8, 31
	v_lshl_add_u64 v[2:3], s[8:9], 1, v[2:3]
	s_mov_b64 s[8:9], 0x5a800000
	v_lshl_add_u64 v[206:207], v[2:3], 0, s[8:9]
	s_lshl_b32 s8, s89, 4
	v_and_or_b32 v0, s8, 48, v0
	s_ashr_i32 s8, s13, 3
	v_lshlrev_b32_e32 v0, 7, v0
	s_andn2_b32 s8, s8, 31
	v_lshlrev_b32_e32 v230, 3, v4
	v_lshl_add_u64 v[2:3], s[10:11], 0, v[0:1]
	s_ashr_i32 s9, s8, 31
	v_and_b32_e32 v234, 24, v230
	v_lshl_add_u64 v[2:3], s[8:9], 1, v[2:3]
	v_lshlrev_b32_e32 v0, 1, v234
	s_lshl_b32 s12, s89, 10
	v_lshl_add_u64 v[2:3], v[2:3], 0, v[0:1]
	s_mov_b64 s[8:9], 0x5cc00000
	s_cmp_lg_u32 0, -1
	v_lshl_add_u64 v[208:209], v[2:3], 0, s[8:9]
	s_cselect_b32 s8, 0, 0
	s_lshl_b32 s70, s69, 7
	s_add_i32 s45, s12, s8
	v_lshl_add_u64 v[34:35], v[206:207], 0, s[70:71]
	s_mov_b32 s8, m0
	s_mov_b32 m0, s45
	s_nop 0
	global_load_lds_dwordx4 v[34:35], off
	s_mov_b32 m0, s8
	s_add_i32 s44, s45, 0x6000
	v_lshl_add_u64 v[2:3], v[208:209], 0, s[70:71]
	s_mov_b32 s8, m0
	s_mov_b32 m0, s44
	s_nop 0
	global_load_lds_dwordx4 v[2:3], off
	s_mov_b32 m0, s8
	s_bitset1_b32 s70, 13
	v_lshlrev_b32_e32 v0, 12, v231
	v_lshl_add_u64 v[2:3], v[206:207], 0, s[70:71]
	s_add_i32 s8, s45, 0x2000
	s_mov_b32 s9, m0
	s_mov_b32 m0, s8
	s_nop 0
	global_load_lds_dwordx4 v[2:3], off
	s_mov_b32 m0, s9
	v_lshl_or_b32 v0, v232, 4, v0
	global_load_dwordx4 v[152:155], v0, s[34:35] nt
	global_load_dwordx4 v[144:147], v0, s[34:35] offset:32 nt
	global_load_dwordx4 v[132:135], v0, s[34:35] offset:64 nt
	global_load_dwordx4 v[128:131], v0, s[34:35] offset:96 nt
	v_mov_b32_e32 v2, v1
	v_mov_b32_e32 v3, v1
	v_mov_b32_e32 v4, v1
	v_mov_b32_e32 v5, v1
	v_mov_b32_e32 v6, v1
	v_mov_b32_e32 v7, v1
	v_mov_b32_e32 v8, v1
	v_mov_b32_e32 v9, v1
	v_mov_b32_e32 v10, v1
	v_mov_b32_e32 v11, v1
	v_mov_b32_e32 v12, v1
	v_mov_b32_e32 v13, v1
	v_mov_b32_e32 v14, v1
	v_mov_b32_e32 v15, v1
	v_lshlrev_b32_e32 v0, 10, v232
	v_lshlrev_b32_e32 v16, 4, v231
	v_add3_u32 v240, 0, v0, v16
	v_mov_b32_e32 v0, v1
	v_mov_b64_e32 v[16:17], v[14:15]
	v_mov_b64_e32 v[14:15], v[12:13]
	v_mov_b64_e32 v[12:13], v[10:11]
	v_mov_b64_e32 v[10:11], v[8:9]
	v_mov_b64_e32 v[8:9], v[6:7]
	v_mov_b64_e32 v[6:7], v[4:5]
	v_mov_b64_e32 v[4:5], v[2:3]
	v_mov_b64_e32 v[2:3], v[0:1]
	s_mov_b64 s[8:9], 0x4000
	v_lshl_add_u64 v[18:19], v[34:35], 0, s[8:9]
	s_add_i32 s8, s45, 0x4000
	s_mov_b32 s9, m0
	s_mov_b32 m0, s8
	s_nop 0
	global_load_lds_dwordx4 v[18:19], off
	s_mov_b32 m0, s9
	s_waitcnt vmcnt(3) lgkmcnt(0)
	s_barrier
	s_waitcnt vmcnt(14)
	ds_read_b128 v[38:41], v240
	v_cndmask_b32_e32 v0, 0, v210, vcc
	v_cmp_nlt_f32_e64 s[8:9], 0, v0
	s_and_b64 vcc, exec, s[8:9]
	s_waitcnt vmcnt(3) lgkmcnt(0)
	v_mfma_f32_32x32x16_bf16 v[18:33], v[38:41], v[152:155], v[2:17]
	ds_read_b128 v[38:41], v240 offset:512
	s_waitcnt lgkmcnt(0)
	v_mfma_f32_32x32x16_bf16 v[2:17], v[38:41], v[152:155], v[2:17]
	ds_read_b128 v[38:41], v240 offset:2048
	s_waitcnt vmcnt(2) lgkmcnt(0)
	v_mfma_f32_32x32x16_bf16 v[18:33], v[38:41], v[144:147], v[18:33]
	ds_read_b128 v[38:41], v240 offset:2560
	s_waitcnt lgkmcnt(0)
	v_mfma_f32_32x32x16_bf16 v[2:17], v[38:41], v[144:147], v[2:17]
	ds_read_b128 v[38:41], v240 offset:4096
	s_waitcnt vmcnt(1) lgkmcnt(0)
	v_mfma_f32_32x32x16_bf16 v[18:33], v[38:41], v[132:135], v[18:33]
	ds_read_b128 v[38:41], v240 offset:4608
	s_waitcnt lgkmcnt(0)
	v_mfma_f32_32x32x16_bf16 v[2:17], v[38:41], v[132:135], v[2:17]
	ds_read_b128 v[38:41], v240 offset:6144
	s_waitcnt vmcnt(0) lgkmcnt(0)
	v_mfma_f32_32x32x16_bf16 v[18:33], v[38:41], v[128:131], v[18:33]
	ds_read_b128 v[38:41], v240 offset:6656
	s_waitcnt lgkmcnt(0)
	v_mfma_f32_32x32x16_bf16 v[2:17], v[38:41], v[128:131], v[2:17]
	s_nop 15
	s_nop 7
	s_cbranch_vccz .LBB0_1065
	v_max3_f32 v37, v18, v19, v2
	v_max3_f32 v38, v20, v21, v3
	s_nop 0
	v_max3_f32 v37, v37, v4, v5
	v_max3_f32 v38, v38, v24, v25
	s_nop 0
	v_max3_f32 v37, v37, v22, v23
	v_max3_f32 v38, v38, v8, v9
	s_nop 0
	v_max3_f32 v37, v37, v6, v7
	v_max3_f32 v38, v38, v28, v29
	s_nop 0
	v_max3_f32 v37, v37, v26, v27
	v_max3_f32 v38, v38, v12, v13
	s_nop 0
	v_max3_f32 v37, v37, v10, v11
	v_max3_f32 v38, v38, v32, v33
	s_nop 0
	v_max3_f32 v37, v37, v30, v31
	v_max3_f32 v38, v38, v16, v17
	s_nop 0
	v_max3_f32 v37, v37, v14, v15
	s_nop 0
	v_max_f32_e32 v37, v37, v38
	s_nop 0
	v_mov_b32_e32 v38, v37
	s_nop 1
	v_permlane32_swap_b32_e32 v37, v38
	v_max_f32_e32 v37, v37, v38
	s_cbranch_execz .LBB0_1066
	s_branch .LBB0_1067
